# baseline (speedup 1.0000x reference)
.LBB2_70:
	s_and_b64 vcc, exec, s[30:31]
	s_cbranch_vccz .LBB2_112
	v_cmp_gt_u32_e64 s[0:1], 10, v0
	s_mov_b32 s25, 0
	s_nop 0
	v_cndmask_b32_e64 v2, 0, v0, s[0:1]
	v_mad_u64_u32 v[2:3], s[2:3], s24, 10, v[2:3]
	v_mov_b32_e32 v3, 0
	s_waitcnt lgkmcnt(0)
	v_lshl_add_u64 v[4:5], v[2:3], 2, s[14:15]
	global_load_dword v6, v[4:5], off
	s_lshl_b64 s[2:3], s[24:25], 2
	s_add_u32 s2, s16, s2
	s_addc_u32 s3, s17, s3
	s_load_dword s14, s[2:3], 0x0
	s_mul_i32 s2, s24, 0x30000
	s_add_u32 s2, s18, s2
	s_addc_u32 s3, s19, 0
	v_lshlrev_b32_e32 v4, 2, v0
	s_add_u32 s38, s2, 0x2000
	s_addc_u32 s39, s3, 0
	global_load_dword v20, v4, s[38:39] offset:-4096 nt
	global_load_dword v22, v4, s[38:39] nt
	s_add_u32 s38, s38, 0x2000
	s_addc_u32 s39, s39, 0
	global_load_dword v18, v4, s[38:39] offset:-4096 nt
	global_load_dword v24, v4, s[38:39] nt
	s_add_u32 s38, s38, 0x2000
	s_addc_u32 s39, s39, 0
	global_load_dword v21, v4, s[38:39] offset:-4096 nt
	global_load_dword v23, v4, s[38:39] nt
	s_add_u32 s38, s38, 0x2000
	s_addc_u32 s39, s39, 0
	global_load_dword v19, v4, s[38:39] offset:-4096 nt
	global_load_dword v25, v4, s[38:39] nt
	s_add_u32 s38, s38, 0x2000
	s_addc_u32 s39, s39, 0
	global_load_dword v29, v4, s[38:39] offset:-4096 nt
	s_add_u32 s38, s38, 0x2000
	s_addc_u32 s39, s39, 0
	global_load_dword v5, v4, s[38:39] offset:-4096 nt
	global_load_dword v26, v4, s[38:39] nt
	s_add_u32 s38, s38, 0x2000
	s_addc_u32 s39, s39, 0
	global_load_dword v31, v4, s[38:39] offset:-4096 nt
	global_load_dword v30, v4, s[38:39] nt
	s_add_u32 s38, s38, 0x2000
	s_addc_u32 s39, s39, 0
	global_load_dword v34, v4, s[38:39] offset:-4096 nt
	global_load_dword v28, v4, s[38:39] nt
	s_add_u32 s38, s38, 0x2000
	s_addc_u32 s39, s39, 0
	global_load_dword v35, v4, s[38:39] offset:-4096 nt
	global_load_dword v42, v4, s[38:39] nt
	s_add_u32 s38, s38, 0x2000
	s_addc_u32 s39, s39, 0
	global_load_dword v46, v4, s[38:39] offset:-4096 nt
	global_load_dword v39, v4, s[38:39] nt
	s_add_u32 s38, s38, 0x2000
	s_addc_u32 s39, s39, 0
	global_load_dword v45, v4, s[38:39] offset:-4096 nt
	s_add_u32 s38, s38, 0x2000
	s_addc_u32 s39, s39, 0
	global_load_dword v27, v4, s[38:39] nt
	s_add_u32 s38, s38, 0x2000
	s_addc_u32 s39, s39, 0
	global_load_dword v33, v4, s[38:39] offset:-4096 nt
	global_load_dword v32, v4, s[38:39] nt
	s_add_u32 s38, s38, 0x2000
	s_addc_u32 s39, s39, 0
	global_load_dword v36, v4, s[38:39] offset:-4096 nt
	global_load_dword v47, v4, s[2:3] nt
	global_load_dword v37, v4, s[38:39] nt
	s_add_u32 s38, s38, 0x2000
	s_addc_u32 s39, s39, 0
	global_load_dword v41, v4, s[38:39] offset:-4096 nt
	global_load_dword v40, v4, s[38:39] nt
	s_add_u32 s38, s38, 0x2000
	s_addc_u32 s39, s39, 0
	global_load_dword v44, v4, s[38:39] offset:-4096 nt
	global_load_dword v38, v4, s[38:39] nt
	s_add_u32 s38, s38, 0x2000
	s_addc_u32 s39, s39, 0
	global_load_dword v43, v4, s[38:39] offset:-4096 nt
	s_waitcnt lgkmcnt(0)
	s_add_i32 s15, s14, 0x7f
	s_and_b32 s15, s15, 0xffffff80
	v_cmp_gt_i32_e32 vcc, s15, v0
	s_nop 1
	s_mov_b64 s[46:47], vcc
	s_and_saveexec_b64 s[6:7], vcc
	s_cbranch_execz .LBB2_85
	s_cmpk_gt_i32 s14, 0x360
	s_cselect_b64 s[8:9], -1, 0
	s_cmpk_lt_i32 s14, 0x361
	s_cbranch_scc1 .LBB2_74
	v_add_u32_e32 v2, 0x24000, v4
	global_load_dword v7, v2, s[2:3]
	v_add_u32_e32 v2, 0x26000, v4
	global_load_dword v8, v2, s[2:3] offset:-4096
	global_load_dword v9, v2, s[2:3]
	v_add_u32_e32 v2, 0x28000, v4
	global_load_dword v10, v2, s[2:3] offset:-4096
	global_load_dword v11, v2, s[2:3]
	v_add_u32_e32 v2, 0x2a000, v4
	global_load_dword v12, v2, s[2:3] offset:-4096
	global_load_dword v13, v2, s[2:3]
	v_add_u32_e32 v2, 0x2c000, v4
	global_load_dword v14, v2, s[2:3] offset:-4096
	global_load_dword v15, v2, s[2:3]
	v_add_u32_e32 v2, 0x2e000, v4
	global_load_dword v16, v2, s[2:3] offset:-4096
